# speedup vs baseline: 1.0577x; 1.0548x over previous
.LBB5_12:
	s_or_b64 exec, exec, s[0:1]
	s_lshl_b32 s0, s42, 9
	s_ashr_i32 s1, s0, 31
	s_lshl_b64 s[0:1], s[0:1], 2
	s_add_u32 s0, s24, s0
	s_addc_u32 s1, s25, s1
	s_lshl_b32 s2, s7, 2
	v_bfe_u32 v153, v0, 6, 2
	s_add_u32 s0, s0, s2
	s_addc_u32 s1, s1, 0
	v_lshlrev_b32_e32 v148, 7, v153
	v_mov_b32_e32 v149, 0
	v_lshl_add_u64 v[10:11], s[0:1], 0, v[148:149]
	v_mov_b32_e32 v147, v149
	v_lshl_add_u64 v[10:11], v[10:11], 0, v[146:147]
	v_and_b32_e32 v254, 48, v0
	v_lshl_add_u32 v254, v153, 7, v254
	v_add_u32_e32 v254, 0x22240, v254
	ds_read_b128 v[34:37], v254
	ds_read_b128 v[26:29], v254 offset:64
	ds_read_b128 v[18:21], v254 offset:512
	ds_read_b128 v[10:13], v254 offset:576
	s_ashr_i32 s35, s34, 31
	s_and_b32 s50, s59, 6
	s_lshl_b64 s[2:3], s[34:35], 3
	s_or_b32 s7, s2, s50
	s_or_b32 s2, s7, s58
	s_lshl_b64 s[24:25], s[2:3], 16
	v_lshrrev_b32_e32 v187, 6, v0
	s_add_u32 s28, s26, s24
	v_and_b32_e32 v157, 4, v187
	s_addc_u32 s29, s27, s25
	s_lshl_b32 s2, s58, 3
	v_lshlrev_b32_e32 v147, 6, v188
	v_lshrrev_b32_e32 v148, 1, v0
	v_lshlrev_b32_e32 v154, 10, v153
	v_lshlrev_b32_e32 v158, 13, v157
	s_cmp_lg_u32 s58, 0
	v_lshl_or_b32 v159, v157, 4, s2
	v_and_or_b32 v155, v148, 24, v147
	v_or_b32_e32 v148, v154, v158
	s_cselect_b64 s[24:25], -1, 0
	v_or_b32_e32 v156, v153, v159
	s_mov_b64 s[0:1], -1
	v_lshl_add_u64 v[150:151], s[28:29], 0, v[148:149]
	v_or_b32_e32 v148, v155, v152
	v_lshl_add_u32 v156, v156, 10, 0
	s_and_b64 vcc, exec, s[24:25]
	s_waitcnt vmcnt(0) lgkmcnt(0)
	s_barrier
	v_lshrrev_b32_e32 v250, 6, v0
	v_and_b32_e32 v251, 63, v0
	s_lshl_b32 s96, s42, 3
	v_or_b32_e32 v250, s96, v250
	v_lshlrev_b32_e32 v250, 16, v250
	v_lshl_add_u32 v250, v251, 4, v250
	s_lshl_b32 s96, s58, 3
	s_and_b32 s97, s33, 6
	s_or_b32 s96, s96, s97
	s_lshl_b32 s96, s96, 12
	s_add_u32 s96, s48, s96
	s_addc_u32 s97, s49, 0
	global_load_dwordx4 v[200:203], v250, s[96:97]
	global_load_dwordx4 v[204:207], v250, s[96:97] offset:1024
	global_load_dwordx4 v[208:211], v250, s[96:97] offset:2048
	global_load_dwordx4 v[212:215], v250, s[96:97] offset:3072
	s_add_u32 s96, s96, 0x1000
	s_addc_u32 s97, s97, 0
	global_load_dwordx4 v[216:219], v250, s[96:97]
	global_load_dwordx4 v[220:223], v250, s[96:97] offset:1024
	global_load_dwordx4 v[224:227], v250, s[96:97] offset:2048
	global_load_dwordx4 v[228:231], v250, s[96:97] offset:3072
	v_and_b32_e32 v232, 15, v0
	v_bfe_u32 v233, v0, 4, 2
	v_lshlrev_b32_e32 v234, 6, v232
	v_lshl_add_u32 v234, v233, 3, v234
	v_lshlrev_b32_e32 v235, 2, v232
	v_and_b32_e32 v235, 32, v235
	v_xor_b32_e32 v234, v234, v235
	v_bfe_u32 v235, v0, 6, 2
	v_lshl_add_u32 v234, v235, 10, v234
	v_lshrrev_b32_e32 v235, 8, v0
	v_lshl_add_u32 v236, v235, 16, v234
	s_lshl_b32 s96, s58, 13
	v_add_u32_e32 v236, s96, v236
	v_xor_b32_e32 v237, 32, v236
	v_lshl_add_u32 v238, v235, 15, v234
	v_xor_b32_e32 v239, 32, v238
	v_add_u32_e32 v239, -8, v239
	v_and_b32_e32 v233, 1, v233
	v_cmp_eq_u32_e32 vcc, 1, v233
	v_cndmask_b32_e32 v238, v238, v239, vcc
	v_mov_b32_e32 v240, 0x3c800000
	v_mov_b32_e32 v241, 0x3c800000
	s_cmp_eq_u32 s58, 0
	s_cbranch_scc1 .Lep_pn0
	v_pk_fma_f32 v[142:143], v[142:143], v[240:241], v[34:35]
	v_pk_fma_f32 v[144:145], v[144:145], v[240:241], v[36:37]
	v_max_f32_e32 v142, 0, v142
	v_max_f32_e32 v143, 0, v143
	v_max_f32_e32 v144, 0, v144
	v_max_f32_e32 v145, 0, v145
	v_cvt_pk_f16_f32 v246, v142, v143
	v_cvt_pk_f16_f32 v247, v144, v145
	v_pk_fma_f32 v[138:139], v[138:139], v[240:241], v[26:27]
	v_pk_fma_f32 v[140:141], v[140:141], v[240:241], v[28:29]
	v_max_f32_e32 v138, 0, v138
	v_max_f32_e32 v139, 0, v139
	v_max_f32_e32 v140, 0, v140
	v_max_f32_e32 v141, 0, v141
	v_cvt_pk_f16_f32 v248, v138, v139
	v_cvt_pk_f16_f32 v249, v140, v141
	s_add_u32 s96, s28, 0x0
	s_addc_u32 s97, s29, 0
	v_permlane16_swap_b32_e32 v246, v248
	v_permlane16_swap_b32_e32 v247, v249
	global_store_dwordx4 v238, v[246:249], s[96:97] sc1
	v_pk_fma_f32 v[134:135], v[134:135], v[240:241], v[18:19]
	v_pk_fma_f32 v[136:137], v[136:137], v[240:241], v[20:21]
	v_max_f32_e32 v134, 0, v134
	v_max_f32_e32 v135, 0, v135
	v_max_f32_e32 v136, 0, v136
	v_max_f32_e32 v137, 0, v137
	v_cvt_pk_f16_f32 v250, v134, v135
	v_cvt_pk_f16_f32 v251, v136, v137
	v_pk_fma_f32 v[130:131], v[130:131], v[240:241], v[10:11]
	v_pk_fma_f32 v[132:133], v[132:133], v[240:241], v[12:13]
	v_max_f32_e32 v130, 0, v130
	v_max_f32_e32 v131, 0, v131
	v_max_f32_e32 v132, 0, v132
	v_max_f32_e32 v133, 0, v133
	v_cvt_pk_f16_f32 v252, v130, v131
	v_cvt_pk_f16_f32 v253, v132, v133
	s_add_u32 s96, s28, 0x1000
	s_addc_u32 s97, s29, 0
	v_permlane16_swap_b32_e32 v250, v252
	v_permlane16_swap_b32_e32 v251, v253
	global_store_dwordx4 v238, v[250:253], s[96:97] sc1
	v_pk_fma_f32 v[126:127], v[126:127], v[240:241], v[34:35]
	v_pk_fma_f32 v[128:129], v[128:129], v[240:241], v[36:37]
	v_max_f32_e32 v126, 0, v126
	v_max_f32_e32 v127, 0, v127
	v_max_f32_e32 v128, 0, v128
	v_max_f32_e32 v129, 0, v129
	v_cvt_pk_f16_f32 v246, v126, v127
	v_cvt_pk_f16_f32 v247, v128, v129
	v_pk_fma_f32 v[122:123], v[122:123], v[240:241], v[26:27]
	v_pk_fma_f32 v[124:125], v[124:125], v[240:241], v[28:29]
	v_max_f32_e32 v122, 0, v122
	v_max_f32_e32 v123, 0, v123
	v_max_f32_e32 v124, 0, v124
	v_max_f32_e32 v125, 0, v125
	v_cvt_pk_f16_f32 v248, v122, v123
	v_cvt_pk_f16_f32 v249, v124, v125
	s_add_u32 s96, s28, 0x2000
	s_addc_u32 s97, s29, 0
	v_permlane16_swap_b32_e32 v246, v248
	v_permlane16_swap_b32_e32 v247, v249
	global_store_dwordx4 v238, v[246:249], s[96:97] sc1
	v_pk_fma_f32 v[118:119], v[118:119], v[240:241], v[18:19]
	v_pk_fma_f32 v[120:121], v[120:121], v[240:241], v[20:21]
	v_max_f32_e32 v118, 0, v118
	v_max_f32_e32 v119, 0, v119
	v_max_f32_e32 v120, 0, v120
	v_max_f32_e32 v121, 0, v121
	v_cvt_pk_f16_f32 v250, v118, v119
	v_cvt_pk_f16_f32 v251, v120, v121
	v_pk_fma_f32 v[114:115], v[114:115], v[240:241], v[10:11]
	v_pk_fma_f32 v[116:117], v[116:117], v[240:241], v[12:13]
	v_max_f32_e32 v114, 0, v114
	v_max_f32_e32 v115, 0, v115
	v_max_f32_e32 v116, 0, v116
	v_max_f32_e32 v117, 0, v117
	v_cvt_pk_f16_f32 v252, v114, v115
	v_cvt_pk_f16_f32 v253, v116, v117
	s_add_u32 s96, s28, 0x3000
	s_addc_u32 s97, s29, 0
	v_permlane16_swap_b32_e32 v250, v252
	v_permlane16_swap_b32_e32 v251, v253
	global_store_dwordx4 v238, v[250:253], s[96:97] sc1
	v_pk_fma_f32 v[110:111], v[110:111], v[240:241], v[34:35]
	v_pk_fma_f32 v[112:113], v[112:113], v[240:241], v[36:37]
	v_max_f32_e32 v110, 0, v110
	v_max_f32_e32 v111, 0, v111
	v_max_f32_e32 v112, 0, v112
	v_max_f32_e32 v113, 0, v113
	v_cvt_pk_f16_f32 v246, v110, v111
	v_cvt_pk_f16_f32 v247, v112, v113
	v_pk_fma_f32 v[106:107], v[106:107], v[240:241], v[26:27]
	v_pk_fma_f32 v[108:109], v[108:109], v[240:241], v[28:29]
	v_max_f32_e32 v106, 0, v106
	v_max_f32_e32 v107, 0, v107
	v_max_f32_e32 v108, 0, v108
	v_max_f32_e32 v109, 0, v109
	v_cvt_pk_f16_f32 v248, v106, v107
	v_cvt_pk_f16_f32 v249, v108, v109
	s_add_u32 s96, s28, 0x4000
	s_addc_u32 s97, s29, 0
	v_permlane16_swap_b32_e32 v246, v248
	v_permlane16_swap_b32_e32 v247, v249
	global_store_dwordx4 v238, v[246:249], s[96:97] sc1
	v_pk_fma_f32 v[102:103], v[102:103], v[240:241], v[18:19]
	v_pk_fma_f32 v[104:105], v[104:105], v[240:241], v[20:21]
	v_max_f32_e32 v102, 0, v102
	v_max_f32_e32 v103, 0, v103
	v_max_f32_e32 v104, 0, v104
	v_max_f32_e32 v105, 0, v105
	v_cvt_pk_f16_f32 v250, v102, v103
	v_cvt_pk_f16_f32 v251, v104, v105
	v_pk_fma_f32 v[98:99], v[98:99], v[240:241], v[10:11]
	v_pk_fma_f32 v[100:101], v[100:101], v[240:241], v[12:13]
	v_max_f32_e32 v98, 0, v98
	v_max_f32_e32 v99, 0, v99
	v_max_f32_e32 v100, 0, v100
	v_max_f32_e32 v101, 0, v101
	v_cvt_pk_f16_f32 v252, v98, v99
	v_cvt_pk_f16_f32 v253, v100, v101
	s_add_u32 s96, s28, 0x5000
	s_addc_u32 s97, s29, 0
	v_permlane16_swap_b32_e32 v250, v252
	v_permlane16_swap_b32_e32 v251, v253
	global_store_dwordx4 v238, v[250:253], s[96:97] sc1
	v_pk_fma_f32 v[94:95], v[94:95], v[240:241], v[34:35]
	v_pk_fma_f32 v[96:97], v[96:97], v[240:241], v[36:37]
	v_max_f32_e32 v94, 0, v94
	v_max_f32_e32 v95, 0, v95
	v_max_f32_e32 v96, 0, v96
	v_max_f32_e32 v97, 0, v97
	v_cvt_pk_f16_f32 v246, v94, v95
	v_cvt_pk_f16_f32 v247, v96, v97
	v_pk_fma_f32 v[90:91], v[90:91], v[240:241], v[26:27]
	v_pk_fma_f32 v[92:93], v[92:93], v[240:241], v[28:29]
	v_max_f32_e32 v90, 0, v90
	v_max_f32_e32 v91, 0, v91
	v_max_f32_e32 v92, 0, v92
	v_max_f32_e32 v93, 0, v93
	v_cvt_pk_f16_f32 v248, v90, v91
	v_cvt_pk_f16_f32 v249, v92, v93
	s_add_u32 s96, s28, 0x6000
	s_addc_u32 s97, s29, 0
	v_permlane16_swap_b32_e32 v246, v248
	v_permlane16_swap_b32_e32 v247, v249
	global_store_dwordx4 v238, v[246:249], s[96:97] sc1
	v_pk_fma_f32 v[86:87], v[86:87], v[240:241], v[18:19]
	v_pk_fma_f32 v[88:89], v[88:89], v[240:241], v[20:21]
	v_max_f32_e32 v86, 0, v86
	v_max_f32_e32 v87, 0, v87
	v_max_f32_e32 v88, 0, v88
	v_max_f32_e32 v89, 0, v89
	v_cvt_pk_f16_f32 v250, v86, v87
	v_cvt_pk_f16_f32 v251, v88, v89
	v_pk_fma_f32 v[82:83], v[82:83], v[240:241], v[10:11]
	v_pk_fma_f32 v[84:85], v[84:85], v[240:241], v[12:13]
	v_max_f32_e32 v82, 0, v82
	v_max_f32_e32 v83, 0, v83
	v_max_f32_e32 v84, 0, v84
	v_max_f32_e32 v85, 0, v85
	v_cvt_pk_f16_f32 v252, v82, v83
	v_cvt_pk_f16_f32 v253, v84, v85
	s_add_u32 s96, s28, 0x7000
	s_addc_u32 s97, s29, 0
	v_permlane16_swap_b32_e32 v250, v252
	v_permlane16_swap_b32_e32 v251, v253
	global_store_dwordx4 v238, v[250:253], s[96:97] sc1
	v_pk_fma_f32 v[78:79], v[78:79], v[240:241], v[34:35]
	v_pk_fma_f32 v[80:81], v[80:81], v[240:241], v[36:37]
	v_max_f32_e32 v78, 0, v78
	v_max_f32_e32 v79, 0, v79
	v_max_f32_e32 v80, 0, v80
	v_max_f32_e32 v81, 0, v81
	v_cvt_pk_f16_f32 v242, v78, v79
	v_cvt_pk_f16_f32 v243, v80, v81
	ds_write_b64 v236, v[242:243] offset:0
	v_pk_fma_f32 v[74:75], v[74:75], v[240:241], v[26:27]
	v_pk_fma_f32 v[76:77], v[76:77], v[240:241], v[28:29]
	v_max_f32_e32 v74, 0, v74
	v_max_f32_e32 v75, 0, v75
	v_max_f32_e32 v76, 0, v76
	v_max_f32_e32 v77, 0, v77
	v_cvt_pk_f16_f32 v244, v74, v75
	v_cvt_pk_f16_f32 v245, v76, v77
	ds_write_b64 v237, v[244:245] offset:0
	v_pk_fma_f32 v[70:71], v[70:71], v[240:241], v[18:19]
	v_pk_fma_f32 v[72:73], v[72:73], v[240:241], v[20:21]
	v_max_f32_e32 v70, 0, v70
	v_max_f32_e32 v71, 0, v71
	v_max_f32_e32 v72, 0, v72
	v_max_f32_e32 v73, 0, v73
	v_cvt_pk_f16_f32 v242, v70, v71
	v_cvt_pk_f16_f32 v243, v72, v73
	ds_write_b64 v236, v[242:243] offset:4096
	v_pk_fma_f32 v[66:67], v[66:67], v[240:241], v[10:11]
	v_pk_fma_f32 v[68:69], v[68:69], v[240:241], v[12:13]
	v_max_f32_e32 v66, 0, v66
	v_max_f32_e32 v67, 0, v67
	v_max_f32_e32 v68, 0, v68
	v_max_f32_e32 v69, 0, v69
	v_cvt_pk_f16_f32 v244, v66, v67
	v_cvt_pk_f16_f32 v245, v68, v69
	ds_write_b64 v237, v[244:245] offset:4096
	v_pk_fma_f32 v[62:63], v[62:63], v[240:241], v[34:35]
	v_pk_fma_f32 v[64:65], v[64:65], v[240:241], v[36:37]
	v_max_f32_e32 v62, 0, v62
	v_max_f32_e32 v63, 0, v63
	v_max_f32_e32 v64, 0, v64
	v_max_f32_e32 v65, 0, v65
	v_cvt_pk_f16_f32 v242, v62, v63
	v_cvt_pk_f16_f32 v243, v64, v65
	ds_write_b64 v236, v[242:243] offset:16384
	v_pk_fma_f32 v[58:59], v[58:59], v[240:241], v[26:27]
	v_pk_fma_f32 v[60:61], v[60:61], v[240:241], v[28:29]
	v_max_f32_e32 v58, 0, v58
	v_max_f32_e32 v59, 0, v59
	v_max_f32_e32 v60, 0, v60
	v_max_f32_e32 v61, 0, v61
	v_cvt_pk_f16_f32 v244, v58, v59
	v_cvt_pk_f16_f32 v245, v60, v61
	ds_write_b64 v237, v[244:245] offset:16384
	v_pk_fma_f32 v[54:55], v[54:55], v[240:241], v[18:19]
	v_pk_fma_f32 v[56:57], v[56:57], v[240:241], v[20:21]
	v_max_f32_e32 v54, 0, v54
	v_max_f32_e32 v55, 0, v55
	v_max_f32_e32 v56, 0, v56
	v_max_f32_e32 v57, 0, v57
	v_cvt_pk_f16_f32 v242, v54, v55
	v_cvt_pk_f16_f32 v243, v56, v57
	ds_write_b64 v236, v[242:243] offset:20480
	v_pk_fma_f32 v[50:51], v[50:51], v[240:241], v[10:11]
	v_pk_fma_f32 v[52:53], v[52:53], v[240:241], v[12:13]
	v_max_f32_e32 v50, 0, v50
	v_max_f32_e32 v51, 0, v51
	v_max_f32_e32 v52, 0, v52
	v_max_f32_e32 v53, 0, v53
	v_cvt_pk_f16_f32 v244, v50, v51
	v_cvt_pk_f16_f32 v245, v52, v53
	ds_write_b64 v237, v[244:245] offset:20480
	v_pk_fma_f32 v[46:47], v[46:47], v[240:241], v[34:35]
	v_pk_fma_f32 v[48:49], v[48:49], v[240:241], v[36:37]
	v_max_f32_e32 v46, 0, v46
	v_max_f32_e32 v47, 0, v47
	v_max_f32_e32 v48, 0, v48
	v_max_f32_e32 v49, 0, v49
	v_cvt_pk_f16_f32 v242, v46, v47
	v_cvt_pk_f16_f32 v243, v48, v49
	ds_write_b64 v236, v[242:243] offset:32768
	v_pk_fma_f32 v[42:43], v[42:43], v[240:241], v[26:27]
	v_pk_fma_f32 v[44:45], v[44:45], v[240:241], v[28:29]
	v_max_f32_e32 v42, 0, v42
	v_max_f32_e32 v43, 0, v43
	v_max_f32_e32 v44, 0, v44
	v_max_f32_e32 v45, 0, v45
	v_cvt_pk_f16_f32 v244, v42, v43
	v_cvt_pk_f16_f32 v245, v44, v45
	ds_write_b64 v237, v[244:245] offset:32768
	v_pk_fma_f32 v[38:39], v[38:39], v[240:241], v[18:19]
	v_pk_fma_f32 v[40:41], v[40:41], v[240:241], v[20:21]
	v_max_f32_e32 v38, 0, v38
	v_max_f32_e32 v39, 0, v39
	v_max_f32_e32 v40, 0, v40
	v_max_f32_e32 v41, 0, v41
	v_cvt_pk_f16_f32 v242, v38, v39
	v_cvt_pk_f16_f32 v243, v40, v41
	ds_write_b64 v236, v[242:243] offset:36864
	v_pk_fma_f32 v[30:31], v[30:31], v[240:241], v[10:11]
	v_pk_fma_f32 v[32:33], v[32:33], v[240:241], v[12:13]
	v_max_f32_e32 v30, 0, v30
	v_max_f32_e32 v31, 0, v31
	v_max_f32_e32 v32, 0, v32
	v_max_f32_e32 v33, 0, v33
	v_cvt_pk_f16_f32 v244, v30, v31
	v_cvt_pk_f16_f32 v245, v32, v33
	ds_write_b64 v237, v[244:245] offset:36864
	v_pk_fma_f32 v[22:23], v[22:23], v[240:241], v[34:35]
	v_pk_fma_f32 v[24:25], v[24:25], v[240:241], v[36:37]
	v_max_f32_e32 v22, 0, v22
	v_max_f32_e32 v23, 0, v23
	v_max_f32_e32 v24, 0, v24
	v_max_f32_e32 v25, 0, v25
	v_cvt_pk_f16_f32 v242, v22, v23
	v_cvt_pk_f16_f32 v243, v24, v25
	ds_write_b64 v236, v[242:243] offset:49152
	v_pk_fma_f32 v[14:15], v[14:15], v[240:241], v[26:27]
	v_pk_fma_f32 v[16:17], v[16:17], v[240:241], v[28:29]
	v_max_f32_e32 v14, 0, v14
	v_max_f32_e32 v15, 0, v15
	v_max_f32_e32 v16, 0, v16
	v_max_f32_e32 v17, 0, v17
	v_cvt_pk_f16_f32 v244, v14, v15
	v_cvt_pk_f16_f32 v245, v16, v17
	ds_write_b64 v237, v[244:245] offset:49152
	v_pk_fma_f32 v[6:7], v[6:7], v[240:241], v[18:19]
	v_pk_fma_f32 v[8:9], v[8:9], v[240:241], v[20:21]
	v_max_f32_e32 v6, 0, v6
	v_max_f32_e32 v7, 0, v7
	v_max_f32_e32 v8, 0, v8
	v_max_f32_e32 v9, 0, v9
	v_cvt_pk_f16_f32 v242, v6, v7
	v_cvt_pk_f16_f32 v243, v8, v9
	ds_write_b64 v236, v[242:243] offset:53248
	v_pk_fma_f32 v[2:3], v[2:3], v[240:241], v[10:11]
	v_pk_fma_f32 v[4:5], v[4:5], v[240:241], v[12:13]
	v_max_f32_e32 v2, 0, v2
	v_max_f32_e32 v3, 0, v3
	v_max_f32_e32 v4, 0, v4
	v_max_f32_e32 v5, 0, v5
	v_cvt_pk_f16_f32 v244, v2, v3
	v_cvt_pk_f16_f32 v245, v4, v5
	ds_write_b64 v237, v[244:245] offset:53248
	s_branch .Lep_done
.Lep_pn0:
	v_pk_fma_f32 v[142:143], v[142:143], v[240:241], v[34:35]
	v_pk_fma_f32 v[144:145], v[144:145], v[240:241], v[36:37]
	v_max_f32_e32 v142, 0, v142
	v_max_f32_e32 v143, 0, v143
	v_max_f32_e32 v144, 0, v144
	v_max_f32_e32 v145, 0, v145
	v_cvt_pk_f16_f32 v242, v142, v143
	v_cvt_pk_f16_f32 v243, v144, v145
	ds_write_b64 v236, v[242:243] offset:0
	v_pk_fma_f32 v[138:139], v[138:139], v[240:241], v[26:27]
	v_pk_fma_f32 v[140:141], v[140:141], v[240:241], v[28:29]
	v_max_f32_e32 v138, 0, v138
	v_max_f32_e32 v139, 0, v139
	v_max_f32_e32 v140, 0, v140
	v_max_f32_e32 v141, 0, v141
	v_cvt_pk_f16_f32 v244, v138, v139
	v_cvt_pk_f16_f32 v245, v140, v141
	ds_write_b64 v237, v[244:245] offset:0
	v_pk_fma_f32 v[134:135], v[134:135], v[240:241], v[18:19]
	v_pk_fma_f32 v[136:137], v[136:137], v[240:241], v[20:21]
	v_max_f32_e32 v134, 0, v134
	v_max_f32_e32 v135, 0, v135
	v_max_f32_e32 v136, 0, v136
	v_max_f32_e32 v137, 0, v137
	v_cvt_pk_f16_f32 v242, v134, v135
	v_cvt_pk_f16_f32 v243, v136, v137
	ds_write_b64 v236, v[242:243] offset:4096
	v_pk_fma_f32 v[130:131], v[130:131], v[240:241], v[10:11]
	v_pk_fma_f32 v[132:133], v[132:133], v[240:241], v[12:13]
	v_max_f32_e32 v130, 0, v130
	v_max_f32_e32 v131, 0, v131
	v_max_f32_e32 v132, 0, v132
	v_max_f32_e32 v133, 0, v133
	v_cvt_pk_f16_f32 v244, v130, v131
	v_cvt_pk_f16_f32 v245, v132, v133
	ds_write_b64 v237, v[244:245] offset:4096
	v_pk_fma_f32 v[126:127], v[126:127], v[240:241], v[34:35]
	v_pk_fma_f32 v[128:129], v[128:129], v[240:241], v[36:37]
	v_max_f32_e32 v126, 0, v126
	v_max_f32_e32 v127, 0, v127
	v_max_f32_e32 v128, 0, v128
	v_max_f32_e32 v129, 0, v129
	v_cvt_pk_f16_f32 v242, v126, v127
	v_cvt_pk_f16_f32 v243, v128, v129
	ds_write_b64 v236, v[242:243] offset:16384
	v_pk_fma_f32 v[122:123], v[122:123], v[240:241], v[26:27]
	v_pk_fma_f32 v[124:125], v[124:125], v[240:241], v[28:29]
	v_max_f32_e32 v122, 0, v122
	v_max_f32_e32 v123, 0, v123
	v_max_f32_e32 v124, 0, v124
	v_max_f32_e32 v125, 0, v125
	v_cvt_pk_f16_f32 v244, v122, v123
	v_cvt_pk_f16_f32 v245, v124, v125
	ds_write_b64 v237, v[244:245] offset:16384
	v_pk_fma_f32 v[118:119], v[118:119], v[240:241], v[18:19]
	v_pk_fma_f32 v[120:121], v[120:121], v[240:241], v[20:21]
	v_max_f32_e32 v118, 0, v118
	v_max_f32_e32 v119, 0, v119
	v_max_f32_e32 v120, 0, v120
	v_max_f32_e32 v121, 0, v121
	v_cvt_pk_f16_f32 v242, v118, v119
	v_cvt_pk_f16_f32 v243, v120, v121
	ds_write_b64 v236, v[242:243] offset:20480
	v_pk_fma_f32 v[114:115], v[114:115], v[240:241], v[10:11]
	v_pk_fma_f32 v[116:117], v[116:117], v[240:241], v[12:13]
	v_max_f32_e32 v114, 0, v114
	v_max_f32_e32 v115, 0, v115
	v_max_f32_e32 v116, 0, v116
	v_max_f32_e32 v117, 0, v117
	v_cvt_pk_f16_f32 v244, v114, v115
	v_cvt_pk_f16_f32 v245, v116, v117
	ds_write_b64 v237, v[244:245] offset:20480
	v_pk_fma_f32 v[110:111], v[110:111], v[240:241], v[34:35]
	v_pk_fma_f32 v[112:113], v[112:113], v[240:241], v[36:37]
	v_max_f32_e32 v110, 0, v110
	v_max_f32_e32 v111, 0, v111
	v_max_f32_e32 v112, 0, v112
	v_max_f32_e32 v113, 0, v113
	v_cvt_pk_f16_f32 v242, v110, v111
	v_cvt_pk_f16_f32 v243, v112, v113
	ds_write_b64 v236, v[242:243] offset:32768
	v_pk_fma_f32 v[106:107], v[106:107], v[240:241], v[26:27]
	v_pk_fma_f32 v[108:109], v[108:109], v[240:241], v[28:29]
	v_max_f32_e32 v106, 0, v106
	v_max_f32_e32 v107, 0, v107
	v_max_f32_e32 v108, 0, v108
	v_max_f32_e32 v109, 0, v109
	v_cvt_pk_f16_f32 v244, v106, v107
	v_cvt_pk_f16_f32 v245, v108, v109
	ds_write_b64 v237, v[244:245] offset:32768
	v_pk_fma_f32 v[102:103], v[102:103], v[240:241], v[18:19]
	v_pk_fma_f32 v[104:105], v[104:105], v[240:241], v[20:21]
	v_max_f32_e32 v102, 0, v102
	v_max_f32_e32 v103, 0, v103
	v_max_f32_e32 v104, 0, v104
	v_max_f32_e32 v105, 0, v105
	v_cvt_pk_f16_f32 v242, v102, v103
	v_cvt_pk_f16_f32 v243, v104, v105
	ds_write_b64 v236, v[242:243] offset:36864
	v_pk_fma_f32 v[98:99], v[98:99], v[240:241], v[10:11]
	v_pk_fma_f32 v[100:101], v[100:101], v[240:241], v[12:13]
	v_max_f32_e32 v98, 0, v98
	v_max_f32_e32 v99, 0, v99
	v_max_f32_e32 v100, 0, v100
	v_max_f32_e32 v101, 0, v101
	v_cvt_pk_f16_f32 v244, v98, v99
	v_cvt_pk_f16_f32 v245, v100, v101
	ds_write_b64 v237, v[244:245] offset:36864
	v_pk_fma_f32 v[94:95], v[94:95], v[240:241], v[34:35]
	v_pk_fma_f32 v[96:97], v[96:97], v[240:241], v[36:37]
	v_max_f32_e32 v94, 0, v94
	v_max_f32_e32 v95, 0, v95
	v_max_f32_e32 v96, 0, v96
	v_max_f32_e32 v97, 0, v97
	v_cvt_pk_f16_f32 v242, v94, v95
	v_cvt_pk_f16_f32 v243, v96, v97
	ds_write_b64 v236, v[242:243] offset:49152
	v_pk_fma_f32 v[90:91], v[90:91], v[240:241], v[26:27]
	v_pk_fma_f32 v[92:93], v[92:93], v[240:241], v[28:29]
	v_max_f32_e32 v90, 0, v90
	v_max_f32_e32 v91, 0, v91
	v_max_f32_e32 v92, 0, v92
	v_max_f32_e32 v93, 0, v93
	v_cvt_pk_f16_f32 v244, v90, v91
	v_cvt_pk_f16_f32 v245, v92, v93
	ds_write_b64 v237, v[244:245] offset:49152
	v_pk_fma_f32 v[86:87], v[86:87], v[240:241], v[18:19]
	v_pk_fma_f32 v[88:89], v[88:89], v[240:241], v[20:21]
	v_max_f32_e32 v86, 0, v86
	v_max_f32_e32 v87, 0, v87
	v_max_f32_e32 v88, 0, v88
	v_max_f32_e32 v89, 0, v89
	v_cvt_pk_f16_f32 v242, v86, v87
	v_cvt_pk_f16_f32 v243, v88, v89
	ds_write_b64 v236, v[242:243] offset:53248
	v_pk_fma_f32 v[82:83], v[82:83], v[240:241], v[10:11]
	v_pk_fma_f32 v[84:85], v[84:85], v[240:241], v[12:13]
	v_max_f32_e32 v82, 0, v82
	v_max_f32_e32 v83, 0, v83
	v_max_f32_e32 v84, 0, v84
	v_max_f32_e32 v85, 0, v85
	v_cvt_pk_f16_f32 v244, v82, v83
	v_cvt_pk_f16_f32 v245, v84, v85
	ds_write_b64 v237, v[244:245] offset:53248
	v_pk_fma_f32 v[78:79], v[78:79], v[240:241], v[34:35]
	v_pk_fma_f32 v[80:81], v[80:81], v[240:241], v[36:37]
	v_max_f32_e32 v78, 0, v78
	v_max_f32_e32 v79, 0, v79
	v_max_f32_e32 v80, 0, v80
	v_max_f32_e32 v81, 0, v81
	v_cvt_pk_f16_f32 v246, v78, v79
	v_cvt_pk_f16_f32 v247, v80, v81
	v_pk_fma_f32 v[74:75], v[74:75], v[240:241], v[26:27]
	v_pk_fma_f32 v[76:77], v[76:77], v[240:241], v[28:29]
	v_max_f32_e32 v74, 0, v74
	v_max_f32_e32 v75, 0, v75
	v_max_f32_e32 v76, 0, v76
	v_max_f32_e32 v77, 0, v77
	v_cvt_pk_f16_f32 v248, v74, v75
	v_cvt_pk_f16_f32 v249, v76, v77
	s_add_u32 s96, s28, 0x0
	s_addc_u32 s97, s29, 0
	v_permlane16_swap_b32_e32 v246, v248
	v_permlane16_swap_b32_e32 v247, v249
	global_store_dwordx4 v238, v[246:249], s[96:97] sc1
	v_pk_fma_f32 v[70:71], v[70:71], v[240:241], v[18:19]
	v_pk_fma_f32 v[72:73], v[72:73], v[240:241], v[20:21]
	v_max_f32_e32 v70, 0, v70
	v_max_f32_e32 v71, 0, v71
	v_max_f32_e32 v72, 0, v72
	v_max_f32_e32 v73, 0, v73
	v_cvt_pk_f16_f32 v250, v70, v71
	v_cvt_pk_f16_f32 v251, v72, v73
	v_pk_fma_f32 v[66:67], v[66:67], v[240:241], v[10:11]
	v_pk_fma_f32 v[68:69], v[68:69], v[240:241], v[12:13]
	v_max_f32_e32 v66, 0, v66
	v_max_f32_e32 v67, 0, v67
	v_max_f32_e32 v68, 0, v68
	v_max_f32_e32 v69, 0, v69
	v_cvt_pk_f16_f32 v252, v66, v67
	v_cvt_pk_f16_f32 v253, v68, v69
	s_add_u32 s96, s28, 0x1000
	s_addc_u32 s97, s29, 0
	v_permlane16_swap_b32_e32 v250, v252
	v_permlane16_swap_b32_e32 v251, v253
	global_store_dwordx4 v238, v[250:253], s[96:97] sc1
	v_pk_fma_f32 v[62:63], v[62:63], v[240:241], v[34:35]
	v_pk_fma_f32 v[64:65], v[64:65], v[240:241], v[36:37]
	v_max_f32_e32 v62, 0, v62
	v_max_f32_e32 v63, 0, v63
	v_max_f32_e32 v64, 0, v64
	v_max_f32_e32 v65, 0, v65
	v_cvt_pk_f16_f32 v246, v62, v63
	v_cvt_pk_f16_f32 v247, v64, v65
	v_pk_fma_f32 v[58:59], v[58:59], v[240:241], v[26:27]
	v_pk_fma_f32 v[60:61], v[60:61], v[240:241], v[28:29]
	v_max_f32_e32 v58, 0, v58
	v_max_f32_e32 v59, 0, v59
	v_max_f32_e32 v60, 0, v60
	v_max_f32_e32 v61, 0, v61
	v_cvt_pk_f16_f32 v248, v58, v59
	v_cvt_pk_f16_f32 v249, v60, v61
	s_add_u32 s96, s28, 0x2000
	s_addc_u32 s97, s29, 0
	v_permlane16_swap_b32_e32 v246, v248
	v_permlane16_swap_b32_e32 v247, v249
	global_store_dwordx4 v238, v[246:249], s[96:97] sc1
	v_pk_fma_f32 v[54:55], v[54:55], v[240:241], v[18:19]
	v_pk_fma_f32 v[56:57], v[56:57], v[240:241], v[20:21]
	v_max_f32_e32 v54, 0, v54
	v_max_f32_e32 v55, 0, v55
	v_max_f32_e32 v56, 0, v56
	v_max_f32_e32 v57, 0, v57
	v_cvt_pk_f16_f32 v250, v54, v55
	v_cvt_pk_f16_f32 v251, v56, v57
	v_pk_fma_f32 v[50:51], v[50:51], v[240:241], v[10:11]
	v_pk_fma_f32 v[52:53], v[52:53], v[240:241], v[12:13]
	v_max_f32_e32 v50, 0, v50
	v_max_f32_e32 v51, 0, v51
	v_max_f32_e32 v52, 0, v52
	v_max_f32_e32 v53, 0, v53
	v_cvt_pk_f16_f32 v252, v50, v51
	v_cvt_pk_f16_f32 v253, v52, v53
	s_add_u32 s96, s28, 0x3000
	s_addc_u32 s97, s29, 0
	v_permlane16_swap_b32_e32 v250, v252
	v_permlane16_swap_b32_e32 v251, v253
	global_store_dwordx4 v238, v[250:253], s[96:97] sc1
	v_pk_fma_f32 v[46:47], v[46:47], v[240:241], v[34:35]
	v_pk_fma_f32 v[48:49], v[48:49], v[240:241], v[36:37]
	v_max_f32_e32 v46, 0, v46
	v_max_f32_e32 v47, 0, v47
	v_max_f32_e32 v48, 0, v48
	v_max_f32_e32 v49, 0, v49
	v_cvt_pk_f16_f32 v246, v46, v47
	v_cvt_pk_f16_f32 v247, v48, v49
	v_pk_fma_f32 v[42:43], v[42:43], v[240:241], v[26:27]
	v_pk_fma_f32 v[44:45], v[44:45], v[240:241], v[28:29]
	v_max_f32_e32 v42, 0, v42
	v_max_f32_e32 v43, 0, v43
	v_max_f32_e32 v44, 0, v44
	v_max_f32_e32 v45, 0, v45
	v_cvt_pk_f16_f32 v248, v42, v43
	v_cvt_pk_f16_f32 v249, v44, v45
	s_add_u32 s96, s28, 0x4000
	s_addc_u32 s97, s29, 0
	v_permlane16_swap_b32_e32 v246, v248
	v_permlane16_swap_b32_e32 v247, v249
	global_store_dwordx4 v238, v[246:249], s[96:97] sc1
	v_pk_fma_f32 v[38:39], v[38:39], v[240:241], v[18:19]
	v_pk_fma_f32 v[40:41], v[40:41], v[240:241], v[20:21]
	v_max_f32_e32 v38, 0, v38
	v_max_f32_e32 v39, 0, v39
	v_max_f32_e32 v40, 0, v40
	v_max_f32_e32 v41, 0, v41
	v_cvt_pk_f16_f32 v250, v38, v39
	v_cvt_pk_f16_f32 v251, v40, v41
	v_pk_fma_f32 v[30:31], v[30:31], v[240:241], v[10:11]
	v_pk_fma_f32 v[32:33], v[32:33], v[240:241], v[12:13]
	v_max_f32_e32 v30, 0, v30
	v_max_f32_e32 v31, 0, v31
	v_max_f32_e32 v32, 0, v32
	v_max_f32_e32 v33, 0, v33
	v_cvt_pk_f16_f32 v252, v30, v31
	v_cvt_pk_f16_f32 v253, v32, v33
	s_add_u32 s96, s28, 0x5000
	s_addc_u32 s97, s29, 0
	v_permlane16_swap_b32_e32 v250, v252
	v_permlane16_swap_b32_e32 v251, v253
	global_store_dwordx4 v238, v[250:253], s[96:97] sc1
	v_pk_fma_f32 v[22:23], v[22:23], v[240:241], v[34:35]
	v_pk_fma_f32 v[24:25], v[24:25], v[240:241], v[36:37]
	v_max_f32_e32 v22, 0, v22
	v_max_f32_e32 v23, 0, v23
	v_max_f32_e32 v24, 0, v24
	v_max_f32_e32 v25, 0, v25
	v_cvt_pk_f16_f32 v246, v22, v23
	v_cvt_pk_f16_f32 v247, v24, v25
	v_pk_fma_f32 v[14:15], v[14:15], v[240:241], v[26:27]
	v_pk_fma_f32 v[16:17], v[16:17], v[240:241], v[28:29]
	v_max_f32_e32 v14, 0, v14
	v_max_f32_e32 v15, 0, v15
	v_max_f32_e32 v16, 0, v16
	v_max_f32_e32 v17, 0, v17
	v_cvt_pk_f16_f32 v248, v14, v15
	v_cvt_pk_f16_f32 v249, v16, v17
	s_add_u32 s96, s28, 0x6000
	s_addc_u32 s97, s29, 0
	v_permlane16_swap_b32_e32 v246, v248
	v_permlane16_swap_b32_e32 v247, v249
	global_store_dwordx4 v238, v[246:249], s[96:97] sc1
	v_pk_fma_f32 v[6:7], v[6:7], v[240:241], v[18:19]
	v_pk_fma_f32 v[8:9], v[8:9], v[240:241], v[20:21]
	v_max_f32_e32 v6, 0, v6
	v_max_f32_e32 v7, 0, v7
	v_max_f32_e32 v8, 0, v8
	v_max_f32_e32 v9, 0, v9
	v_cvt_pk_f16_f32 v250, v6, v7
	v_cvt_pk_f16_f32 v251, v8, v9
	v_pk_fma_f32 v[2:3], v[2:3], v[240:241], v[10:11]
	v_pk_fma_f32 v[4:5], v[4:5], v[240:241], v[12:13]
	v_max_f32_e32 v2, 0, v2
	v_max_f32_e32 v3, 0, v3
	v_max_f32_e32 v4, 0, v4
	v_max_f32_e32 v5, 0, v5
	v_cvt_pk_f16_f32 v252, v2, v3
	v_cvt_pk_f16_f32 v253, v4, v5
	s_add_u32 s96, s28, 0x7000
	s_addc_u32 s97, s29, 0
	v_permlane16_swap_b32_e32 v250, v252
	v_permlane16_swap_b32_e32 v251, v253
	global_store_dwordx4 v238, v[250:253], s[96:97] sc1

.LBB5_140:
	v_lshl_or_b32 v2, s42, 3, v187
	v_ashrrev_i32_e32 v3, 31, v2
	v_lshlrev_b64 v[2:3], 16, v[2:3]
	v_lshl_add_u64 v[2:3], s[48:49], 0, v[2:3]
	v_mov_b32_e32 v169, 0
	v_lshlrev_b32_e32 v168, 4, v189
	s_or_b32 s25, s2, s50
	s_or_b32 s24, s50, 1
	s_mov_b32 s1, 0
	v_lshl_add_u64 v[166:167], v[2:3], 0, v[168:169]
	s_lshl_b32 s0, s25, 12
	s_or_b32 s30, s2, s24
	v_lshl_add_u64 v[18:19], v[166:167], 0, s[0:1]
	s_lshl_b32 s0, s30, 12
	v_lshl_add_u64 v[34:35], v[166:167], 0, s[0:1]
	s_waitcnt vmcnt(8)
	v_mov_b32_e32 v2, v200
	v_mov_b32_e32 v3, v201
	v_mov_b32_e32 v4, v202
	v_mov_b32_e32 v5, v203
	v_mov_b32_e32 v6, v204
	v_mov_b32_e32 v7, v205
	v_mov_b32_e32 v8, v206
	v_mov_b32_e32 v9, v207
	v_mov_b32_e32 v10, v208
	v_mov_b32_e32 v11, v209
	v_mov_b32_e32 v12, v210
	v_mov_b32_e32 v13, v211
	v_mov_b32_e32 v14, v212
	v_mov_b32_e32 v15, v213
	v_mov_b32_e32 v16, v214
	v_mov_b32_e32 v17, v215
	v_mov_b32_e32 v18, v216
	v_mov_b32_e32 v19, v217
	v_mov_b32_e32 v20, v218
	v_mov_b32_e32 v21, v219
	v_mov_b32_e32 v22, v220
	v_mov_b32_e32 v23, v221
	v_mov_b32_e32 v24, v222
	v_mov_b32_e32 v25, v223
	v_mov_b32_e32 v26, v224
	v_mov_b32_e32 v27, v225
	v_mov_b32_e32 v28, v226
	v_mov_b32_e32 v29, v227
	v_mov_b32_e32 v30, v228
	v_mov_b32_e32 v31, v229
	v_mov_b32_e32 v32, v230
	v_mov_b32_e32 v33, v231
	v_or_b32_e32 v52, v147, v146
	s_add_i32 s0, s59, 2
	s_and_b32 s28, s0, 6
	s_or_b32 s31, s2, s28
	s_lshl_b32 s0, s31, 12
	v_lshl_add_u64 v[50:51], v[166:167], 0, s[0:1]
	s_waitcnt lgkmcnt(0)
	s_barrier
	global_load_dwordx4 v[34:37], v[50:51], off
	global_load_dwordx4 v[38:41], v[50:51], off offset:1024
	global_load_dwordx4 v[42:45], v[50:51], off offset:2048
	global_load_dwordx4 v[46:49], v[50:51], off offset:3072
	v_xad_u32 v191, v52, v152, 0
	v_lshl_add_u32 v122, s25, 10, v191
	ds_read_b128 v[50:53], v122
	ds_read_b128 v[54:57], v122 offset:16384
	ds_read_b128 v[58:61], v122 offset:32768
	ds_read_b128 v[62:65], v122 offset:49152
	s_setprio 1
	s_waitcnt vmcnt(19) lgkmcnt(3)
	v_mfma_f32_16x16x32_f16 v[66:69], v[2:5], v[50:53], 0
	s_waitcnt vmcnt(18)
	v_mfma_f32_16x16x32_f16 v[70:73], v[6:9], v[50:53], 0
	s_waitcnt vmcnt(17)
	v_mfma_f32_16x16x32_f16 v[74:77], v[10:13], v[50:53], 0
	s_waitcnt vmcnt(16)
	v_mfma_f32_16x16x32_f16 v[50:53], v[14:17], v[50:53], 0
	s_waitcnt lgkmcnt(2)
	v_mfma_f32_16x16x32_f16 v[78:81], v[2:5], v[54:57], 0
	v_mfma_f32_16x16x32_f16 v[82:85], v[6:9], v[54:57], 0
	v_mfma_f32_16x16x32_f16 v[86:89], v[10:13], v[54:57], 0
	v_mfma_f32_16x16x32_f16 v[54:57], v[14:17], v[54:57], 0
	s_waitcnt lgkmcnt(1)
	v_mfma_f32_16x16x32_f16 v[90:93], v[2:5], v[58:61], 0
	v_mfma_f32_16x16x32_f16 v[94:97], v[6:9], v[58:61], 0
	v_mfma_f32_16x16x32_f16 v[98:101], v[10:13], v[58:61], 0
	v_mfma_f32_16x16x32_f16 v[58:61], v[14:17], v[58:61], 0
	s_waitcnt lgkmcnt(0)
	v_mfma_f32_16x16x32_f16 v[102:105], v[2:5], v[62:65], 0
	v_mfma_f32_16x16x32_f16 v[106:109], v[6:9], v[62:65], 0
	v_mfma_f32_16x16x32_f16 v[110:113], v[10:13], v[62:65], 0
	v_mfma_f32_16x16x32_f16 v[62:65], v[14:17], v[62:65], 0
	s_setprio 0
	v_add_u32_e32 v114, 0x10000, v122
	v_add_u32_e32 v118, 0x14000, v122
	v_add_u32_e32 v123, 0x18000, v122
	v_add_u32_e32 v126, 0x1c000, v122
	ds_read_b128 v[114:117], v114
	ds_read_b128 v[118:121], v118
	ds_read_b128 v[122:125], v123
	ds_read_b128 v[126:129], v126
	s_setprio 1
	s_waitcnt lgkmcnt(3)
	v_mfma_f32_16x16x32_f16 v[130:133], v[2:5], v[114:117], 0
	v_mfma_f32_16x16x32_f16 v[134:137], v[6:9], v[114:117], 0
	v_mfma_f32_16x16x32_f16 v[138:141], v[10:13], v[114:117], 0
	v_mfma_f32_16x16x32_f16 v[114:117], v[14:17], v[114:117], 0
	s_waitcnt lgkmcnt(2)
	v_mfma_f32_16x16x32_f16 v[142:145], v[2:5], v[118:121], 0
	v_mfma_f32_16x16x32_f16 v[146:149], v[6:9], v[118:121], 0
	v_mfma_f32_16x16x32_f16 v[150:153], v[10:13], v[118:121], 0
	v_mfma_f32_16x16x32_f16 v[118:121], v[14:17], v[118:121], 0
	s_waitcnt lgkmcnt(1)
	v_mfma_f32_16x16x32_f16 v[154:157], v[2:5], v[122:125], 0
	v_mfma_f32_16x16x32_f16 v[158:161], v[6:9], v[122:125], 0
	v_mfma_f32_16x16x32_f16 v[170:173], v[10:13], v[122:125], 0
	v_mfma_f32_16x16x32_f16 v[122:125], v[14:17], v[122:125], 0
	s_waitcnt lgkmcnt(0)
	v_mfma_f32_16x16x32_f16 v[2:5], v[2:5], v[126:129], 0
	v_mfma_f32_16x16x32_f16 v[6:9], v[6:9], v[126:129], 0
	v_mfma_f32_16x16x32_f16 v[10:13], v[10:13], v[126:129], 0
	v_mfma_f32_16x16x32_f16 v[14:17], v[14:17], v[126:129], 0
	s_setprio 0
	s_add_i32 s0, s50, 3
	s_and_b32 s29, s0, 7
	s_or_b32 s48, s29, s2
	s_lshl_b32 s0, s48, 12
	v_lshl_add_u64 v[178:179], v[166:167], 0, s[0:1]
	global_load_dwordx4 v[126:129], v[178:179], off
	global_load_dwordx4 v[174:177], v[178:179], off offset:1024
	global_load_dwordx4 v[192:195], v[178:179], off offset:2048
	global_load_dwordx4 v[196:199], v[178:179], off offset:3072
	v_lshl_add_u32 v163, s30, 10, v191
	ds_read_b128 v[200:203], v163
	ds_read_b128 v[204:207], v163 offset:16384
	ds_read_b128 v[208:211], v163 offset:32768
	ds_read_b128 v[212:215], v163 offset:49152
	s_setprio 1
	s_waitcnt vmcnt(19) lgkmcnt(3)
	v_mfma_f32_16x16x32_f16 v[66:69], v[18:21], v[200:203], v[66:69]
	s_waitcnt vmcnt(18)
	v_mfma_f32_16x16x32_f16 v[70:73], v[22:25], v[200:203], v[70:73]
	s_waitcnt vmcnt(17)
	v_mfma_f32_16x16x32_f16 v[74:77], v[26:29], v[200:203], v[74:77]
	s_waitcnt vmcnt(16)
	v_mfma_f32_16x16x32_f16 v[50:53], v[30:33], v[200:203], v[50:53]
	s_waitcnt lgkmcnt(2)
	v_mfma_f32_16x16x32_f16 v[78:81], v[18:21], v[204:207], v[78:81]
	v_mfma_f32_16x16x32_f16 v[82:85], v[22:25], v[204:207], v[82:85]
	v_mfma_f32_16x16x32_f16 v[86:89], v[26:29], v[204:207], v[86:89]
	v_mfma_f32_16x16x32_f16 v[54:57], v[30:33], v[204:207], v[54:57]
	s_waitcnt lgkmcnt(1)
	v_mfma_f32_16x16x32_f16 v[90:93], v[18:21], v[208:211], v[90:93]
	v_mfma_f32_16x16x32_f16 v[94:97], v[22:25], v[208:211], v[94:97]
	v_mfma_f32_16x16x32_f16 v[98:101], v[26:29], v[208:211], v[98:101]
	v_mfma_f32_16x16x32_f16 v[58:61], v[30:33], v[208:211], v[58:61]
	s_waitcnt lgkmcnt(0)
	v_mfma_f32_16x16x32_f16 v[102:105], v[18:21], v[212:215], v[102:105]
	v_mfma_f32_16x16x32_f16 v[106:109], v[22:25], v[212:215], v[106:109]
	v_mfma_f32_16x16x32_f16 v[110:113], v[26:29], v[212:215], v[110:113]
	v_mfma_f32_16x16x32_f16 v[62:65], v[30:33], v[212:215], v[62:65]
	s_setprio 0
	v_add_u32_e32 v165, 0x10000, v163
	v_add_u32_e32 v168, 0x14000, v163
	ds_read_b128 v[200:203], v165
	ds_read_b128 v[204:207], v168
	v_add_u32_e32 v165, 0x18000, v163
	v_add_u32_e32 v163, 0x1c000, v163
	ds_read_b128 v[208:211], v165
	ds_read_b128 v[212:215], v163
	s_setprio 1
	s_waitcnt lgkmcnt(3)
	v_mfma_f32_16x16x32_f16 v[130:133], v[18:21], v[200:203], v[130:133]
	v_mfma_f32_16x16x32_f16 v[134:137], v[22:25], v[200:203], v[134:137]
	v_mfma_f32_16x16x32_f16 v[138:141], v[26:29], v[200:203], v[138:141]
	v_mfma_f32_16x16x32_f16 v[114:117], v[30:33], v[200:203], v[114:117]
	s_waitcnt lgkmcnt(2)
	v_mfma_f32_16x16x32_f16 v[142:145], v[18:21], v[204:207], v[142:145]
	v_mfma_f32_16x16x32_f16 v[146:149], v[22:25], v[204:207], v[146:149]
	v_mfma_f32_16x16x32_f16 v[150:153], v[26:29], v[204:207], v[150:153]
	v_mfma_f32_16x16x32_f16 v[118:121], v[30:33], v[204:207], v[118:121]
	s_waitcnt lgkmcnt(1)
	v_mfma_f32_16x16x32_f16 v[154:157], v[18:21], v[208:211], v[154:157]
	v_mfma_f32_16x16x32_f16 v[158:161], v[22:25], v[208:211], v[158:161]
	v_mfma_f32_16x16x32_f16 v[122:125], v[30:33], v[208:211], v[122:125]
	s_waitcnt lgkmcnt(0)
	v_mfma_f32_16x16x32_f16 v[2:5], v[18:21], v[212:215], v[2:5]
	v_mfma_f32_16x16x32_f16 v[6:9], v[22:25], v[212:215], v[6:9]
	v_mfma_f32_16x16x32_f16 v[10:13], v[26:29], v[212:215], v[10:13]
	v_mfma_f32_16x16x32_f16 v[14:17], v[30:33], v[212:215], v[14:17]
	v_mfma_f32_16x16x32_f16 v[170:173], v[26:29], v[208:211], v[170:173]
	s_setprio 0
	s_xor_b32 s25, s25, 4
	s_lshl_b32 s0, s25, 12
	v_lshl_add_u64 v[30:31], v[166:167], 0, s[0:1]
	s_waitcnt vmcnt(8)
	s_barrier
	s_getreg_b32 s80, hwreg(HW_REG_XCC_ID, 0, 4)
	s_and_b32 s80, s80, 15
	s_add_i32 s80, s80, 1
	s_lshl_b32 s81, s34, 3
	s_or_b32 s81, s81, s33
	s_lshl_b32 s81, s81, 7
	s_add_u32 s82, s46, s81
	s_addc_u32 s83, s47, 0
	v_mov_b32_e32 v254, 0
	v_mov_b32_e32 v255, s80
	s_and_saveexec_b64 s[84:85], s[4:5]
	global_store_dword v254, v255, s[82:83] sc1
	s_mov_b64 exec, s[84:85]
	global_load_dwordx4 v[18:21], v[30:31], off
	global_load_dwordx4 v[22:25], v[30:31], off offset:1024
	global_load_dwordx4 v[26:29], v[30:31], off offset:2048
	s_nop 0
	global_load_dwordx4 v[30:33], v[30:31], off offset:3072
	v_lshl_add_u32 v163, s31, 10, v191
	ds_read_b128 v[200:203], v163
	ds_read_b128 v[204:207], v163 offset:16384
	ds_read_b128 v[208:211], v163 offset:32768
	ds_read_b128 v[212:215], v163 offset:49152
	s_setprio 1
	s_waitcnt vmcnt(11) lgkmcnt(3)
	v_mfma_f32_16x16x32_f16 v[66:69], v[34:37], v[200:203], v[66:69]
	s_waitcnt vmcnt(10)
	v_mfma_f32_16x16x32_f16 v[70:73], v[38:41], v[200:203], v[70:73]
	s_waitcnt vmcnt(9)
	v_mfma_f32_16x16x32_f16 v[74:77], v[42:45], v[200:203], v[74:77]
	s_waitcnt vmcnt(8)
	v_mfma_f32_16x16x32_f16 v[50:53], v[46:49], v[200:203], v[50:53]
	s_waitcnt lgkmcnt(2)
	v_mfma_f32_16x16x32_f16 v[78:81], v[34:37], v[204:207], v[78:81]
	v_mfma_f32_16x16x32_f16 v[82:85], v[38:41], v[204:207], v[82:85]
	v_mfma_f32_16x16x32_f16 v[86:89], v[42:45], v[204:207], v[86:89]
	v_mfma_f32_16x16x32_f16 v[54:57], v[46:49], v[204:207], v[54:57]
	s_waitcnt lgkmcnt(1)
	v_mfma_f32_16x16x32_f16 v[90:93], v[34:37], v[208:211], v[90:93]
	v_mfma_f32_16x16x32_f16 v[94:97], v[38:41], v[208:211], v[94:97]
	v_mfma_f32_16x16x32_f16 v[98:101], v[42:45], v[208:211], v[98:101]
	v_mfma_f32_16x16x32_f16 v[58:61], v[46:49], v[208:211], v[58:61]
	s_waitcnt lgkmcnt(0)
	v_mfma_f32_16x16x32_f16 v[102:105], v[34:37], v[212:215], v[102:105]
	v_mfma_f32_16x16x32_f16 v[106:109], v[38:41], v[212:215], v[106:109]
	v_mfma_f32_16x16x32_f16 v[110:113], v[42:45], v[212:215], v[110:113]
	v_mfma_f32_16x16x32_f16 v[62:65], v[46:49], v[212:215], v[62:65]
	s_setprio 0
	v_add_u32_e32 v165, 0x10000, v163
	v_add_u32_e32 v168, 0x14000, v163
	ds_read_b128 v[200:203], v165
	ds_read_b128 v[204:207], v168
	v_add_u32_e32 v165, 0x18000, v163
	v_add_u32_e32 v163, 0x1c000, v163
	ds_read_b128 v[208:211], v165
	ds_read_b128 v[212:215], v163
	s_setprio 1
	s_waitcnt lgkmcnt(3)
	v_mfma_f32_16x16x32_f16 v[130:133], v[34:37], v[200:203], v[130:133]
	v_mfma_f32_16x16x32_f16 v[134:137], v[38:41], v[200:203], v[134:137]
	v_mfma_f32_16x16x32_f16 v[138:141], v[42:45], v[200:203], v[138:141]
	v_mfma_f32_16x16x32_f16 v[114:117], v[46:49], v[200:203], v[114:117]
	s_waitcnt lgkmcnt(2)
	v_mfma_f32_16x16x32_f16 v[142:145], v[34:37], v[204:207], v[142:145]
	v_mfma_f32_16x16x32_f16 v[146:149], v[38:41], v[204:207], v[146:149]
	v_mfma_f32_16x16x32_f16 v[150:153], v[42:45], v[204:207], v[150:153]
	v_mfma_f32_16x16x32_f16 v[118:121], v[46:49], v[204:207], v[118:121]
	s_waitcnt lgkmcnt(1)
	v_mfma_f32_16x16x32_f16 v[154:157], v[34:37], v[208:211], v[154:157]
	v_mfma_f32_16x16x32_f16 v[158:161], v[38:41], v[208:211], v[158:161]
	v_mfma_f32_16x16x32_f16 v[122:125], v[46:49], v[208:211], v[122:125]
	s_waitcnt lgkmcnt(0)
	v_mfma_f32_16x16x32_f16 v[2:5], v[34:37], v[212:215], v[2:5]
	v_mfma_f32_16x16x32_f16 v[6:9], v[38:41], v[212:215], v[6:9]
	v_mfma_f32_16x16x32_f16 v[10:13], v[42:45], v[212:215], v[10:13]
	v_mfma_f32_16x16x32_f16 v[14:17], v[46:49], v[212:215], v[14:17]
	v_mfma_f32_16x16x32_f16 v[170:173], v[42:45], v[208:211], v[170:173]
	s_setprio 0
	s_add_i32 s0, s50, 5
	s_and_b32 s30, s0, 7
	s_or_b32 s49, s30, s2
	s_lshl_b32 s0, s49, 12
	v_lshl_add_u64 v[46:47], v[166:167], 0, s[0:1]
	global_load_dwordx4 v[34:37], v[46:47], off
	global_load_dwordx4 v[38:41], v[46:47], off offset:1024
	global_load_dwordx4 v[42:45], v[46:47], off offset:2048
	s_nop 0
	global_load_dwordx4 v[46:49], v[46:47], off offset:3072
	v_lshl_add_u32 v163, s48, 10, v191
	ds_read_b128 v[200:203], v163
	ds_read_b128 v[204:207], v163 offset:16384
	ds_read_b128 v[208:211], v163 offset:32768
	ds_read_b128 v[212:215], v163 offset:49152
	s_setprio 1
	s_waitcnt vmcnt(11) lgkmcnt(3)
	v_mfma_f32_16x16x32_f16 v[66:69], v[126:129], v[200:203], v[66:69]
	s_waitcnt vmcnt(10)
	v_mfma_f32_16x16x32_f16 v[70:73], v[174:177], v[200:203], v[70:73]
	s_waitcnt vmcnt(9)
	v_mfma_f32_16x16x32_f16 v[74:77], v[192:195], v[200:203], v[74:77]
	s_waitcnt vmcnt(8)
	v_mfma_f32_16x16x32_f16 v[50:53], v[196:199], v[200:203], v[50:53]
	s_waitcnt lgkmcnt(2)
	v_mfma_f32_16x16x32_f16 v[78:81], v[126:129], v[204:207], v[78:81]
	v_mfma_f32_16x16x32_f16 v[82:85], v[174:177], v[204:207], v[82:85]
	v_mfma_f32_16x16x32_f16 v[86:89], v[192:195], v[204:207], v[86:89]
	v_mfma_f32_16x16x32_f16 v[54:57], v[196:199], v[204:207], v[54:57]
	s_waitcnt lgkmcnt(1)
	v_mfma_f32_16x16x32_f16 v[90:93], v[126:129], v[208:211], v[90:93]
	v_mfma_f32_16x16x32_f16 v[94:97], v[174:177], v[208:211], v[94:97]
	v_mfma_f32_16x16x32_f16 v[98:101], v[192:195], v[208:211], v[98:101]
	v_mfma_f32_16x16x32_f16 v[58:61], v[196:199], v[208:211], v[58:61]
	s_waitcnt lgkmcnt(0)
	v_mfma_f32_16x16x32_f16 v[102:105], v[126:129], v[212:215], v[102:105]
	v_mfma_f32_16x16x32_f16 v[106:109], v[174:177], v[212:215], v[106:109]
	v_mfma_f32_16x16x32_f16 v[110:113], v[192:195], v[212:215], v[110:113]
	v_mfma_f32_16x16x32_f16 v[62:65], v[196:199], v[212:215], v[62:65]
	s_setprio 0
	v_add_u32_e32 v165, 0x10000, v163
	v_add_u32_e32 v168, 0x14000, v163
	ds_read_b128 v[200:203], v165
	ds_read_b128 v[204:207], v168
	v_add_u32_e32 v165, 0x18000, v163
	v_add_u32_e32 v163, 0x1c000, v163
	ds_read_b128 v[208:211], v165
	ds_read_b128 v[212:215], v163
	s_setprio 1
	s_waitcnt lgkmcnt(3)
	v_mfma_f32_16x16x32_f16 v[130:133], v[126:129], v[200:203], v[130:133]
	v_mfma_f32_16x16x32_f16 v[134:137], v[174:177], v[200:203], v[134:137]
	v_mfma_f32_16x16x32_f16 v[138:141], v[192:195], v[200:203], v[138:141]
	v_mfma_f32_16x16x32_f16 v[114:117], v[196:199], v[200:203], v[114:117]
	s_waitcnt lgkmcnt(2)
	v_mfma_f32_16x16x32_f16 v[142:145], v[126:129], v[204:207], v[142:145]
	v_mfma_f32_16x16x32_f16 v[146:149], v[174:177], v[204:207], v[146:149]
	v_mfma_f32_16x16x32_f16 v[150:153], v[192:195], v[204:207], v[150:153]
	v_mfma_f32_16x16x32_f16 v[118:121], v[196:199], v[204:207], v[118:121]
	s_waitcnt lgkmcnt(1)
	v_mfma_f32_16x16x32_f16 v[154:157], v[126:129], v[208:211], v[154:157]
	v_mfma_f32_16x16x32_f16 v[158:161], v[174:177], v[208:211], v[158:161]
	v_mfma_f32_16x16x32_f16 v[122:125], v[196:199], v[208:211], v[122:125]
	s_waitcnt lgkmcnt(0)
	v_mfma_f32_16x16x32_f16 v[2:5], v[126:129], v[212:215], v[2:5]
	v_mfma_f32_16x16x32_f16 v[6:9], v[174:177], v[212:215], v[6:9]
	v_mfma_f32_16x16x32_f16 v[10:13], v[192:195], v[212:215], v[10:13]
	v_mfma_f32_16x16x32_f16 v[14:17], v[196:199], v[212:215], v[14:17]
	v_mfma_f32_16x16x32_f16 v[170:173], v[192:195], v[208:211], v[170:173]
	s_setprio 0
	s_add_i32 s59, s59, 6
	s_and_b32 s31, s59, 6
	s_or_b32 s52, s2, s31
	s_lshl_b32 s0, s52, 12
	v_lshl_add_u64 v[178:179], v[166:167], 0, s[0:1]
	s_lshl_b32 s86, s34, 3
	s_or_b32 s86, s86, s33
	s_xor_b32 s86, s86, 1
	s_lshl_b32 s86, s86, 7
	s_add_u32 s86, s46, s86
	s_addc_u32 s87, s47, 0
	v_mov_b32_e32 v254, 0
	global_load_dword v254, v254, s[86:87] sc1
	global_load_dwordx4 v[126:129], v[178:179], off
	global_load_dwordx4 v[174:177], v[178:179], off offset:1024
	global_load_dwordx4 v[192:195], v[178:179], off offset:2048
	global_load_dwordx4 v[196:199], v[178:179], off offset:3072
	v_lshl_add_u32 v163, s25, 10, v191
	ds_read_b128 v[200:203], v163
	ds_read_b128 v[204:207], v163 offset:16384
	ds_read_b128 v[208:211], v163 offset:32768
	ds_read_b128 v[212:215], v163 offset:49152
	s_setprio 1
	s_waitcnt vmcnt(12) lgkmcnt(3)
	v_mfma_f32_16x16x32_f16 v[66:69], v[18:21], v[200:203], v[66:69]
	s_waitcnt vmcnt(11)
	v_mfma_f32_16x16x32_f16 v[70:73], v[22:25], v[200:203], v[70:73]
	s_waitcnt vmcnt(10)
	v_mfma_f32_16x16x32_f16 v[74:77], v[26:29], v[200:203], v[74:77]
	s_waitcnt vmcnt(9)
	v_mfma_f32_16x16x32_f16 v[50:53], v[30:33], v[200:203], v[50:53]
	s_waitcnt lgkmcnt(2)
	v_mfma_f32_16x16x32_f16 v[78:81], v[18:21], v[204:207], v[78:81]
	v_mfma_f32_16x16x32_f16 v[82:85], v[22:25], v[204:207], v[82:85]
	v_mfma_f32_16x16x32_f16 v[86:89], v[26:29], v[204:207], v[86:89]
	v_mfma_f32_16x16x32_f16 v[54:57], v[30:33], v[204:207], v[54:57]
	s_waitcnt lgkmcnt(1)
	v_mfma_f32_16x16x32_f16 v[90:93], v[18:21], v[208:211], v[90:93]
	v_mfma_f32_16x16x32_f16 v[94:97], v[22:25], v[208:211], v[94:97]
	v_mfma_f32_16x16x32_f16 v[98:101], v[26:29], v[208:211], v[98:101]
	v_mfma_f32_16x16x32_f16 v[58:61], v[30:33], v[208:211], v[58:61]
	s_waitcnt lgkmcnt(0)
	v_mfma_f32_16x16x32_f16 v[102:105], v[18:21], v[212:215], v[102:105]
	v_mfma_f32_16x16x32_f16 v[106:109], v[22:25], v[212:215], v[106:109]
	v_mfma_f32_16x16x32_f16 v[110:113], v[26:29], v[212:215], v[110:113]
	v_mfma_f32_16x16x32_f16 v[62:65], v[30:33], v[212:215], v[62:65]
	s_setprio 0
	v_add_u32_e32 v165, 0x10000, v163
	v_add_u32_e32 v168, 0x14000, v163
	ds_read_b128 v[200:203], v165
	ds_read_b128 v[204:207], v168
	v_add_u32_e32 v165, 0x18000, v163
	v_add_u32_e32 v163, 0x1c000, v163
	ds_read_b128 v[208:211], v165
	ds_read_b128 v[212:215], v163
	s_setprio 1
	s_waitcnt lgkmcnt(3)
	v_mfma_f32_16x16x32_f16 v[130:133], v[18:21], v[200:203], v[130:133]
	v_mfma_f32_16x16x32_f16 v[134:137], v[22:25], v[200:203], v[134:137]
	v_mfma_f32_16x16x32_f16 v[138:141], v[26:29], v[200:203], v[138:141]
	v_mfma_f32_16x16x32_f16 v[114:117], v[30:33], v[200:203], v[114:117]
	s_waitcnt lgkmcnt(2)
	v_mfma_f32_16x16x32_f16 v[142:145], v[18:21], v[204:207], v[142:145]
	v_mfma_f32_16x16x32_f16 v[146:149], v[22:25], v[204:207], v[146:149]
	v_mfma_f32_16x16x32_f16 v[150:153], v[26:29], v[204:207], v[150:153]
	v_mfma_f32_16x16x32_f16 v[118:121], v[30:33], v[204:207], v[118:121]
	s_waitcnt lgkmcnt(1)
	v_mfma_f32_16x16x32_f16 v[154:157], v[18:21], v[208:211], v[154:157]
	v_mfma_f32_16x16x32_f16 v[158:161], v[22:25], v[208:211], v[158:161]
	v_mfma_f32_16x16x32_f16 v[122:125], v[30:33], v[208:211], v[122:125]
	s_waitcnt lgkmcnt(0)
	v_mfma_f32_16x16x32_f16 v[2:5], v[18:21], v[212:215], v[2:5]
	v_mfma_f32_16x16x32_f16 v[6:9], v[22:25], v[212:215], v[6:9]
	v_mfma_f32_16x16x32_f16 v[10:13], v[26:29], v[212:215], v[10:13]
	v_mfma_f32_16x16x32_f16 v[14:17], v[30:33], v[212:215], v[14:17]
	v_mfma_f32_16x16x32_f16 v[170:173], v[26:29], v[208:211], v[170:173]
	s_setprio 0
	s_add_i32 s0, s50, -1
	s_and_b32 s48, s0, 7
	s_or_b32 s25, s48, s2
	s_lshl_b32 s0, s25, 12
	v_lshl_add_u64 v[18:19], v[166:167], 0, s[0:1]
	global_load_dwordx4 v[200:203], v[18:19], off
	global_load_dwordx4 v[204:207], v[18:19], off offset:1024
	global_load_dwordx4 v[208:211], v[18:19], off offset:2048
	global_load_dwordx4 v[212:215], v[18:19], off offset:3072
	v_lshl_add_u32 v163, s49, 10, v191
	ds_read_b128 v[18:21], v163
	ds_read_b128 v[22:25], v163 offset:16384
	ds_read_b128 v[26:29], v163 offset:32768
	ds_read_b128 v[30:33], v163 offset:49152
	s_setprio 1
	s_waitcnt vmcnt(12) lgkmcnt(3)
	v_mfma_f32_16x16x32_f16 v[66:69], v[34:37], v[18:21], v[66:69]
	s_waitcnt vmcnt(11)
	v_mfma_f32_16x16x32_f16 v[70:73], v[38:41], v[18:21], v[70:73]
	s_waitcnt vmcnt(10)
	v_mfma_f32_16x16x32_f16 v[74:77], v[42:45], v[18:21], v[74:77]
	s_waitcnt vmcnt(9)
	v_mfma_f32_16x16x32_f16 v[18:21], v[46:49], v[18:21], v[50:53]
	s_waitcnt lgkmcnt(2)
	v_mfma_f32_16x16x32_f16 v[50:53], v[34:37], v[22:25], v[78:81]
	v_mfma_f32_16x16x32_f16 v[78:81], v[38:41], v[22:25], v[82:85]
	v_mfma_f32_16x16x32_f16 v[82:85], v[42:45], v[22:25], v[86:89]
	v_mfma_f32_16x16x32_f16 v[22:25], v[46:49], v[22:25], v[54:57]
	s_waitcnt lgkmcnt(1)
	v_mfma_f32_16x16x32_f16 v[54:57], v[34:37], v[26:29], v[90:93]
	v_mfma_f32_16x16x32_f16 v[86:89], v[38:41], v[26:29], v[94:97]
	v_mfma_f32_16x16x32_f16 v[90:93], v[42:45], v[26:29], v[98:101]
	v_mfma_f32_16x16x32_f16 v[26:29], v[46:49], v[26:29], v[58:61]
	s_waitcnt lgkmcnt(0)
	v_mfma_f32_16x16x32_f16 v[58:61], v[34:37], v[30:33], v[102:105]
	v_mfma_f32_16x16x32_f16 v[94:97], v[38:41], v[30:33], v[106:109]
	v_mfma_f32_16x16x32_f16 v[98:101], v[42:45], v[30:33], v[110:113]
	v_mfma_f32_16x16x32_f16 v[30:33], v[46:49], v[30:33], v[62:65]
	s_setprio 0
	s_nop 1
	v_add_u32_e32 v62, 0x10000, v163
	v_add_u32_e32 v102, 0x14000, v163
	v_add_u32_e32 v106, 0x18000, v163
	v_add_u32_e32 v110, 0x1c000, v163
	ds_read_b128 v[62:65], v62
	ds_read_b128 v[102:105], v102
	ds_read_b128 v[106:109], v106
	ds_read_b128 v[110:113], v110
	s_setprio 1
	s_waitcnt lgkmcnt(3)
	v_mfma_f32_16x16x32_f16 v[130:133], v[34:37], v[62:65], v[130:133]
	v_mfma_f32_16x16x32_f16 v[134:137], v[38:41], v[62:65], v[134:137]
	v_mfma_f32_16x16x32_f16 v[138:141], v[42:45], v[62:65], v[138:141]
	v_mfma_f32_16x16x32_f16 v[62:65], v[46:49], v[62:65], v[114:117]
	s_waitcnt lgkmcnt(2)
	v_mfma_f32_16x16x32_f16 v[114:117], v[34:37], v[102:105], v[142:145]
	v_mfma_f32_16x16x32_f16 v[142:145], v[38:41], v[102:105], v[146:149]
	v_mfma_f32_16x16x32_f16 v[146:149], v[42:45], v[102:105], v[150:153]
	v_mfma_f32_16x16x32_f16 v[102:105], v[46:49], v[102:105], v[118:121]
	s_waitcnt lgkmcnt(1)
	v_mfma_f32_16x16x32_f16 v[118:121], v[34:37], v[106:109], v[154:157]
	v_mfma_f32_16x16x32_f16 v[150:153], v[38:41], v[106:109], v[158:161]
	v_mfma_f32_16x16x32_f16 v[154:157], v[42:45], v[106:109], v[170:173]
	v_mfma_f32_16x16x32_f16 v[106:109], v[46:49], v[106:109], v[122:125]
	s_waitcnt lgkmcnt(0)
	v_mfma_f32_16x16x32_f16 v[34:37], v[34:37], v[110:113], v[2:5]
	v_mfma_f32_16x16x32_f16 v[38:41], v[38:41], v[110:113], v[6:9]
	v_mfma_f32_16x16x32_f16 v[42:45], v[42:45], v[110:113], v[10:13]
	v_mfma_f32_16x16x32_f16 v[46:49], v[46:49], v[110:113], v[14:17]
	s_setprio 0
	s_xor_b32 s2, s58, 1
	s_lshl_b32 s49, s2, 3
	s_or_b32 s51, s49, s50
	s_lshl_b32 s0, s51, 12
	v_lshl_add_u64 v[14:15], v[166:167], 0, s[0:1]
	s_waitcnt vmcnt(8)
	s_barrier
	v_lshlrev_b32_e32 v255, 4, v0
	v_readfirstlane_b32 s92, v0
	s_lshl_b32 s92, s92, 4
	s_xor_b32 s93, s58, 1
	s_lshl_b32 s94, s93, 13
	s_add_i32 s92, s92, s94
	s_lshl_b32 s94, s34, 3
	s_or_b32 s94, s94, s33
	s_xor_b32 s94, s94, 1
	s_lshl_b32 s94, s94, 16
	s_add_u32 s88, s26, s94
	s_addc_u32 s89, s27, 0
	s_add_i32 s95, s92, 0x0
	s_mov_b32 m0, s95
	s_add_u32 s84, s88, 0x0
	s_addc_u32 s85, s89, 0
	global_load_lds_dwordx4 v255, s[84:85] sc0 sc1
	s_add_i32 s95, s92, 0x4000
	s_mov_b32 m0, s95
	s_add_u32 s84, s88, 0x2000
	s_addc_u32 s85, s89, 0
	global_load_lds_dwordx4 v255, s[84:85] sc0 sc1
	s_add_i32 s95, s92, 0x8000
	s_mov_b32 m0, s95
	s_add_u32 s84, s88, 0x4000
	s_addc_u32 s85, s89, 0
	global_load_lds_dwordx4 v255, s[84:85] sc0 sc1
	s_add_i32 s95, s92, 0xc000
	s_mov_b32 m0, s95
	s_add_u32 s84, s88, 0x6000
	s_addc_u32 s85, s89, 0
	global_load_lds_dwordx4 v255, s[84:85] sc0 sc1
	s_add_i32 s95, s92, 0x10000
	s_mov_b32 m0, s95
	s_add_u32 s84, s88, 0x8000
	s_addc_u32 s85, s89, 0
	global_load_lds_dwordx4 v255, s[84:85] sc0 sc1
	s_add_i32 s95, s92, 0x14000
	s_mov_b32 m0, s95
	s_add_u32 s84, s88, 0xa000
	s_addc_u32 s85, s89, 0
	global_load_lds_dwordx4 v255, s[84:85] sc0 sc1
	s_add_i32 s95, s92, 0x18000
	s_mov_b32 m0, s95
	s_add_u32 s84, s88, 0xc000
	s_addc_u32 s85, s89, 0
	global_load_lds_dwordx4 v255, s[84:85] sc0 sc1
	s_add_i32 s95, s92, 0x1c000
	s_mov_b32 m0, s95
	s_add_u32 s84, s88, 0xe000
	s_addc_u32 s85, s89, 0
	global_load_lds_dwordx4 v255, s[84:85] sc0 sc1
	global_load_dwordx4 v[2:5], v[14:15], off
	global_load_dwordx4 v[6:9], v[14:15], off offset:1024
	global_load_dwordx4 v[10:13], v[14:15], off offset:2048
	s_nop 0
	global_load_dwordx4 v[14:17], v[14:15], off offset:3072
	v_lshl_add_u32 v163, s52, 10, v191
	ds_read_b128 v[110:113], v163
	ds_read_b128 v[122:125], v163 offset:16384
	ds_read_b128 v[158:161], v163 offset:32768
	ds_read_b128 v[170:173], v163 offset:49152
	s_setprio 1
	s_waitcnt vmcnt(19) lgkmcnt(3)
	v_mfma_f32_16x16x32_f16 v[66:69], v[126:129], v[110:113], v[66:69]
	s_waitcnt vmcnt(18)
	v_mfma_f32_16x16x32_f16 v[70:73], v[174:177], v[110:113], v[70:73]
	s_waitcnt vmcnt(17)
	v_mfma_f32_16x16x32_f16 v[74:77], v[192:195], v[110:113], v[74:77]
	s_waitcnt vmcnt(16)
	v_mfma_f32_16x16x32_f16 v[110:113], v[196:199], v[110:113], v[18:21]
	s_waitcnt lgkmcnt(2)
	v_mfma_f32_16x16x32_f16 v[50:53], v[126:129], v[122:125], v[50:53]
	v_mfma_f32_16x16x32_f16 v[78:81], v[174:177], v[122:125], v[78:81]
	v_mfma_f32_16x16x32_f16 v[82:85], v[192:195], v[122:125], v[82:85]
	v_mfma_f32_16x16x32_f16 v[122:125], v[196:199], v[122:125], v[22:25]
	s_waitcnt lgkmcnt(1)
	v_mfma_f32_16x16x32_f16 v[216:219], v[126:129], v[158:161], v[54:57]
	v_mfma_f32_16x16x32_f16 v[86:89], v[174:177], v[158:161], v[86:89]
	v_mfma_f32_16x16x32_f16 v[90:93], v[192:195], v[158:161], v[90:93]
	v_mfma_f32_16x16x32_f16 v[158:161], v[196:199], v[158:161], v[26:29]
	s_waitcnt lgkmcnt(0)
	v_mfma_f32_16x16x32_f16 v[94:97], v[174:177], v[170:173], v[94:97]
	v_mfma_f32_16x16x32_f16 v[98:101], v[192:195], v[170:173], v[98:101]
	v_mfma_f32_16x16x32_f16 v[220:223], v[126:129], v[170:173], v[58:61]
	v_mfma_f32_16x16x32_f16 v[170:173], v[196:199], v[170:173], v[30:33]
	s_setprio 0
	v_add_u32_e32 v18, 0x10000, v163
	v_add_u32_e32 v22, 0x14000, v163
	v_add_u32_e32 v26, 0x18000, v163
	v_add_u32_e32 v30, 0x1c000, v163
	ds_read_b128 v[18:21], v18
	ds_read_b128 v[22:25], v22
	ds_read_b128 v[26:29], v26
	ds_read_b128 v[30:33], v30
	s_setprio 1
	s_waitcnt lgkmcnt(3)
	v_mfma_f32_16x16x32_f16 v[130:133], v[126:129], v[18:21], v[130:133]
	v_mfma_f32_16x16x32_f16 v[134:137], v[174:177], v[18:21], v[134:137]
	v_mfma_f32_16x16x32_f16 v[138:141], v[192:195], v[18:21], v[138:141]
	s_waitcnt lgkmcnt(2)
	v_mfma_f32_16x16x32_f16 v[114:117], v[126:129], v[22:25], v[114:117]
	v_mfma_f32_16x16x32_f16 v[142:145], v[174:177], v[22:25], v[142:145]
	v_mfma_f32_16x16x32_f16 v[146:149], v[192:195], v[22:25], v[146:149]
	s_waitcnt lgkmcnt(1)
	v_mfma_f32_16x16x32_f16 v[150:153], v[174:177], v[26:29], v[150:153]
	v_mfma_f32_16x16x32_f16 v[154:157], v[192:195], v[26:29], v[154:157]
	v_mfma_f32_16x16x32_f16 v[224:227], v[196:199], v[18:21], v[62:65]
	v_mfma_f32_16x16x32_f16 v[228:231], v[196:199], v[22:25], v[102:105]
	v_mfma_f32_16x16x32_f16 v[232:235], v[126:129], v[26:29], v[118:121]
	v_mfma_f32_16x16x32_f16 v[236:239], v[196:199], v[26:29], v[106:109]
	s_waitcnt lgkmcnt(0)
	v_mfma_f32_16x16x32_f16 v[240:243], v[126:129], v[30:33], v[34:37]
	v_mfma_f32_16x16x32_f16 v[174:177], v[174:177], v[30:33], v[38:41]
	v_mfma_f32_16x16x32_f16 v[192:195], v[192:195], v[30:33], v[42:45]
	v_mfma_f32_16x16x32_f16 v[196:199], v[196:199], v[30:33], v[46:49]
	s_setprio 0
	s_or_b32 s52, s49, s24
	s_lshl_b32 s0, s52, 12
	v_lshl_add_u64 v[30:31], v[166:167], 0, s[0:1]
	global_load_dwordx4 v[18:21], v[30:31], off
	global_load_dwordx4 v[22:25], v[30:31], off offset:1024
	global_load_dwordx4 v[26:29], v[30:31], off offset:2048
	s_nop 0
	global_load_dwordx4 v[30:33], v[30:31], off offset:3072
	v_lshl_add_u32 v118, s25, 10, v191
	ds_read_b128 v[46:49], v118
	ds_read_b128 v[62:65], v118 offset:16384
	ds_read_b128 v[102:105], v118 offset:32768
	ds_read_b128 v[106:109], v118 offset:49152
	s_setprio 1
	s_waitcnt vmcnt(19) lgkmcnt(3)
	v_mfma_f32_16x16x32_f16 v[34:37], v[200:203], v[46:49], v[66:69]
	s_waitcnt vmcnt(18)
	v_mfma_f32_16x16x32_f16 v[38:41], v[204:207], v[46:49], v[70:73]
	s_waitcnt vmcnt(17)
	v_mfma_f32_16x16x32_f16 v[42:45], v[208:211], v[46:49], v[74:77]
	s_waitcnt vmcnt(16)
	v_mfma_f32_16x16x32_f16 v[46:49], v[212:215], v[46:49], v[110:113]
	s_waitcnt lgkmcnt(2)
	v_mfma_f32_16x16x32_f16 v[50:53], v[200:203], v[62:65], v[50:53]
	v_mfma_f32_16x16x32_f16 v[54:57], v[204:207], v[62:65], v[78:81]
	v_mfma_f32_16x16x32_f16 v[58:61], v[208:211], v[62:65], v[82:85]
	v_mfma_f32_16x16x32_f16 v[62:65], v[212:215], v[62:65], v[122:125]
	s_waitcnt lgkmcnt(1)
	v_mfma_f32_16x16x32_f16 v[66:69], v[200:203], v[102:105], v[216:219]
	v_mfma_f32_16x16x32_f16 v[70:73], v[204:207], v[102:105], v[86:89]
	v_mfma_f32_16x16x32_f16 v[74:77], v[208:211], v[102:105], v[90:93]
	v_mfma_f32_16x16x32_f16 v[78:81], v[212:215], v[102:105], v[158:161]
	s_waitcnt lgkmcnt(0)
	v_mfma_f32_16x16x32_f16 v[82:85], v[200:203], v[106:109], v[220:223]
	v_mfma_f32_16x16x32_f16 v[86:89], v[204:207], v[106:109], v[94:97]
	v_mfma_f32_16x16x32_f16 v[90:93], v[208:211], v[106:109], v[98:101]
	v_mfma_f32_16x16x32_f16 v[94:97], v[212:215], v[106:109], v[170:173]
	s_setprio 0
	s_nop 0
	v_add_u32_e32 v98, 0x10000, v118
	v_add_u32_e32 v99, 0x14000, v118
	ds_read_b128 v[110:113], v98
	ds_read_b128 v[126:129], v99
	v_add_u32_e32 v98, 0x18000, v118
	v_add_u32_e32 v99, 0x1c000, v118
	ds_read_b128 v[158:161], v98
	ds_read_b128 v[170:173], v99
	s_setprio 1
	s_waitcnt lgkmcnt(3)
	v_mfma_f32_16x16x32_f16 v[98:101], v[200:203], v[110:113], v[130:133]
	v_mfma_f32_16x16x32_f16 v[102:105], v[204:207], v[110:113], v[134:137]
	v_mfma_f32_16x16x32_f16 v[106:109], v[208:211], v[110:113], v[138:141]
	v_mfma_f32_16x16x32_f16 v[110:113], v[212:215], v[110:113], v[224:227]
	s_waitcnt lgkmcnt(2)
	v_mfma_f32_16x16x32_f16 v[114:117], v[200:203], v[126:129], v[114:117]
	v_mfma_f32_16x16x32_f16 v[118:121], v[204:207], v[126:129], v[142:145]
	v_mfma_f32_16x16x32_f16 v[122:125], v[208:211], v[126:129], v[146:149]
	v_mfma_f32_16x16x32_f16 v[126:129], v[212:215], v[126:129], v[228:231]
	s_waitcnt lgkmcnt(1)
	v_mfma_f32_16x16x32_f16 v[130:133], v[200:203], v[158:161], v[232:235]
	v_mfma_f32_16x16x32_f16 v[134:137], v[204:207], v[158:161], v[150:153]
	v_mfma_f32_16x16x32_f16 v[138:141], v[208:211], v[158:161], v[154:157]
	v_mfma_f32_16x16x32_f16 v[142:145], v[212:215], v[158:161], v[236:239]
	s_waitcnt lgkmcnt(0)
	v_mfma_f32_16x16x32_f16 v[146:149], v[200:203], v[170:173], v[240:243]
	v_mfma_f32_16x16x32_f16 v[150:153], v[204:207], v[170:173], v[174:177]
	v_mfma_f32_16x16x32_f16 v[154:157], v[208:211], v[170:173], v[192:195]
	v_mfma_f32_16x16x32_f16 v[158:161], v[212:215], v[170:173], v[196:199]
	s_setprio 0
	s_waitcnt vmcnt(0)
	s_barrier
	s_getreg_b32 s24, hwreg(HW_REG_XCC_ID, 0, 4)
	s_and_saveexec_b64 s[0:1], s[4:5]
	s_cbranch_execz .LBB5_145
	s_and_b32 s53, s24, 15
	s_lshl_b32 s24, s34, 3
	s_or_b32 s50, s24, s50
	s_or_b32 s24, s50, s58
	s_lshl_b32 s24, s24, 5
	s_ashr_i32 s25, s24, 31
	s_lshl_b64 s[24:25], s[24:25], 2
	s_add_u32 s24, s46, s24
	s_addc_u32 s25, s47, s25
	s_add_i32 s54, s53, 1
	v_mov_b32_e32 v163, s54
	s_or_b32 s24, s50, s2
	s_lshl_b32 s24, s24, 5
	s_ashr_i32 s25, s24, 31
	s_lshl_b64 s[24:25], s[24:25], 2
	s_add_u32 s24, s46, s24
	s_addc_u32 s25, s47, s25
	s_mov_b32 s90, 0
	v_mov_b32_e32 v163, v254
	v_cmp_ne_u32_e32 vcc, 0, v163
	s_cbranch_vccnz .LBB5_144
	s_mov_b32 s90, 2
	v_mov_b32_e32 v165, 0
